# speedup vs baseline: 1.0487x; 1.0487x over previous
.LBB0_3:
	s_load_dwordx8 s[12:19], s[0:1], 0x0
	s_load_dwordx2 s[20:21], s[0:1], 0x20
	s_load_dwordx8 s[4:11], s[0:1], 0x30
	s_cmpk_gt_u32 s2, 0x407
	s_mov_b64 s[0:1], -1
	s_cbranch_scc0 .LBB0_20
	s_cmpk_gt_u32 s2, 0x887
	s_cbranch_scc0 .LBB0_6
	s_mov_b32 s3, 0
	s_lshl_b64 s[0:1], s[2:3], 2
	s_waitcnt lgkmcnt(0)
	s_add_u32 s4, s4, s0
	s_addc_u32 s5, s5, s1
	s_add_u32 s4, s4, 0xffffdde0
	s_addc_u32 s5, s5, -1
	s_add_u32 s0, s6, s0
	s_addc_u32 s1, s7, s1
	s_add_u32 s0, s0, 0xffffddc0
	s_addc_u32 s1, s1, -1
	s_cmpk_lt_u32 s2, 0x890
	s_cselect_b32 s1, s5, s1
	s_cselect_b32 s0, s4, s0
	v_lshlrev_b32_e32 v2, 5, v0
	v_mov_b32_e32 v3, 0
	v_lshl_add_u64 v[4:5], s[0:1], 0, v[2:3]
	s_movk_i32 s4, 0x2000
	v_add_co_u32_e32 v6, vcc, s4, v4
	s_movk_i32 s4, 0x4000
	s_nop 0
	v_addc_co_u32_e32 v7, vcc, 0, v5, vcc
	v_add_co_u32_e32 v8, vcc, s4, v4
	s_movk_i32 s4, 0x6000
	s_nop 0
	v_addc_co_u32_e32 v9, vcc, 0, v5, vcc
	v_add_co_u32_e32 v4, vcc, s4, v4
	s_nop 1
	v_addc_co_u32_e32 v5, vcc, 0, v5, vcc
	global_load_dword v1, v2, s[0:1] nt
	global_load_dword v3, v[6:7], off nt
	global_load_dword v10, v[8:9], off nt
	global_load_dword v11, v[4:5], off nt
	s_mov_b32 s1, s3
	s_add_i32 s0, s2, 0x978
	s_lshl_b64 s[0:1], s[0:1], 11
	s_add_u32 s0, s10, s0
	v_lshlrev_b32_e32 v2, 1, v0
	s_addc_u32 s1, s11, s1
	s_waitcnt vmcnt(3)
	v_cvt_f16_f32_e32 v1, v1
	s_waitcnt vmcnt(2)
	v_cvt_f16_f32_e32 v3, v3
	s_waitcnt vmcnt(1)
	v_cvt_f16_f32_e32 v4, v10
	s_waitcnt vmcnt(0)
	v_cvt_f16_f32_e32 v5, v11
	global_store_short v2, v1, s[0:1]
	global_store_short v2, v3, s[0:1] offset:512
	global_store_short v2, v4, s[0:1] offset:1024
	global_store_short v2, v5, s[0:1] offset:1536
	s_mov_b64 s[0:1], 0
.LBB0_6:
	s_andn2_b64 vcc, exec, s[0:1]
	s_cbranch_vccnz .LBB0_19
	s_cmpk_gt_u32 s2, 0x4c7
	s_mov_b64 s[0:1], -1
	s_cbranch_scc0 .LBB0_17
	s_cmpk_gt_u32 s2, 0x587
	s_cbranch_scc0 .LBB0_14
	v_lshrrev_b32_e32 v5, 6, v0
	v_and_b32_e32 v2, 63, v0
	v_mul_u32_u24_e32 v1, 0x104, v5
	s_cmpk_gt_u32 s2, 0x707
	v_mov_b32_e32 v3, 0
	v_lshl_add_u32 v1, v2, 2, v1
	v_or_b32_e32 v4, 4, v5
	v_lshlrev_b32_e32 v2, 2, v2
	s_cbranch_scc0 .LBB0_11
	s_add_i32 s0, s2, 0xf8f8
	s_and_b32 s1, s0, 0xffff
	s_mul_i32 s1, s1, 0xaaab
	s_lshr_b32 s1, s1, 20
	s_mul_i32 s3, s1, 24
	s_sub_i32 s0, s0, s3
	s_lshl_b32 s0, s0, 6
	s_and_b32 s0, s0, 0xffc0
	s_lshl_b32 s3, s1, 6
	s_waitcnt lgkmcnt(0)
	s_lshl_b32 s4, s0, 2
	s_add_u32 s4, s20, s4
	v_or_b32_e32 v24, s3, v5
	s_addc_u32 s5, s21, 0
	v_mul_u32_u24_e32 v8, 0x600, v24
	v_or_b32_e32 v10, s3, v4
	v_or_b32_e32 v12, 8, v24
	v_or_b32_e32 v14, 12, v24
	v_or_b32_e32 v16, 16, v24
	v_or_b32_e32 v18, 20, v24
	v_or_b32_e32 v20, 24, v24
	v_or_b32_e32 v22, 28, v24
	v_lshl_add_u64 v[6:7], s[4:5], 0, v[2:3]
	v_lshlrev_b32_e32 v8, 2, v8
	v_mov_b32_e32 v9, v3
	v_mul_u32_u24_e32 v10, 0x600, v10
	v_mul_u32_u24_e32 v12, 0x600, v12
	v_mul_u32_u24_e32 v14, 0x600, v14
	v_mul_u32_u24_e32 v16, 0x600, v16
	v_mul_u32_u24_e32 v18, 0x600, v18
	v_mul_u32_u24_e32 v20, 0x600, v20
	v_mul_u32_u24_e32 v22, 0x600, v22
	v_lshl_add_u64 v[8:9], v[6:7], 0, v[8:9]
	v_lshlrev_b32_e32 v10, 2, v10
	v_mov_b32_e32 v11, v3
	v_lshlrev_b32_e32 v12, 2, v12
	v_mov_b32_e32 v13, v3
	v_lshlrev_b32_e32 v14, 2, v14
	v_mov_b32_e32 v15, v3
	v_lshlrev_b32_e32 v16, 2, v16
	v_mov_b32_e32 v17, v3
	v_lshlrev_b32_e32 v18, 2, v18
	v_mov_b32_e32 v19, v3
	v_lshlrev_b32_e32 v20, 2, v20
	v_mov_b32_e32 v21, v3
	v_lshlrev_b32_e32 v22, 2, v22
	v_mov_b32_e32 v23, v3
	v_lshl_add_u64 v[10:11], v[6:7], 0, v[10:11]
	v_lshl_add_u64 v[12:13], v[6:7], 0, v[12:13]
	v_lshl_add_u64 v[14:15], v[6:7], 0, v[14:15]
	v_lshl_add_u64 v[16:17], v[6:7], 0, v[16:17]
	v_lshl_add_u64 v[18:19], v[6:7], 0, v[18:19]
	v_lshl_add_u64 v[20:21], v[6:7], 0, v[20:21]
	v_lshl_add_u64 v[22:23], v[6:7], 0, v[22:23]
	global_load_dword v25, v[8:9], off nt
	global_load_dword v26, v[10:11], off nt
	global_load_dword v27, v[12:13], off nt
	global_load_dword v28, v[14:15], off nt
	global_load_dword v29, v[16:17], off nt
	global_load_dword v30, v[18:19], off nt
	global_load_dword v31, v[20:21], off nt
	global_load_dword v32, v[22:23], off nt
	v_or_b32_e32 v8, 32, v24
	v_mul_u32_u24_e32 v8, 0x600, v8
	v_or_b32_e32 v10, 36, v24
	v_or_b32_e32 v12, 40, v24
	v_or_b32_e32 v14, 44, v24
	v_or_b32_e32 v16, 48, v24
	v_or_b32_e32 v18, 52, v24
	v_or_b32_e32 v20, 56, v24
	v_or_b32_e32 v22, 60, v24
	v_lshlrev_b32_e32 v8, 2, v8
	v_mov_b32_e32 v9, v3
	v_mul_u32_u24_e32 v10, 0x600, v10
	v_mul_u32_u24_e32 v12, 0x600, v12
	v_mul_u32_u24_e32 v14, 0x600, v14
	v_mul_u32_u24_e32 v16, 0x600, v16
	v_mul_u32_u24_e32 v18, 0x600, v18
	v_mul_u32_u24_e32 v20, 0x600, v20
	v_mul_u32_u24_e32 v22, 0x600, v22
	v_lshl_add_u64 v[8:9], v[6:7], 0, v[8:9]
	v_lshlrev_b32_e32 v10, 2, v10
	v_mov_b32_e32 v11, v3
	v_lshlrev_b32_e32 v12, 2, v12
	v_mov_b32_e32 v13, v3
	v_lshlrev_b32_e32 v14, 2, v14
	v_mov_b32_e32 v15, v3
	v_lshlrev_b32_e32 v16, 2, v16
	v_mov_b32_e32 v17, v3
	v_lshlrev_b32_e32 v18, 2, v18
	v_mov_b32_e32 v19, v3
	v_lshlrev_b32_e32 v20, 2, v20
	v_mov_b32_e32 v21, v3
	v_lshlrev_b32_e32 v22, 2, v22
	v_mov_b32_e32 v23, v3
	v_lshl_add_u64 v[10:11], v[6:7], 0, v[10:11]
	v_lshl_add_u64 v[12:13], v[6:7], 0, v[12:13]
	v_lshl_add_u64 v[14:15], v[6:7], 0, v[14:15]
	v_lshl_add_u64 v[16:17], v[6:7], 0, v[16:17]
	v_lshl_add_u64 v[18:19], v[6:7], 0, v[18:19]
	v_lshl_add_u64 v[20:21], v[6:7], 0, v[20:21]
	v_lshl_add_u64 v[6:7], v[6:7], 0, v[22:23]
	global_load_dword v22, v[8:9], off nt
	global_load_dword v23, v[10:11], off nt
	global_load_dword v24, v[12:13], off nt
	global_load_dword v33, v[14:15], off nt
	global_load_dword v34, v[16:17], off nt
	global_load_dword v35, v[18:19], off nt
	global_load_dword v36, v[20:21], off nt
	global_load_dword v37, v[6:7], off nt
	v_lshlrev_b32_e32 v6, 3, v0
	v_and_b32_e32 v8, 56, v6
	s_waitcnt vmcnt(15)
	ds_write_b32 v1, v25
	s_waitcnt vmcnt(14)
	ds_write_b32 v1, v26 offset:1040
	s_waitcnt vmcnt(13)
	ds_write_b32 v1, v27 offset:2080
	s_waitcnt vmcnt(12)
	ds_write_b32 v1, v28 offset:3120
	s_waitcnt vmcnt(11)
	ds_write_b32 v1, v29 offset:4160
	s_waitcnt vmcnt(10)
	ds_write_b32 v1, v30 offset:5200
	s_waitcnt vmcnt(9)
	ds_write_b32 v1, v31 offset:6240
	s_waitcnt vmcnt(8)
	ds_write_b32 v1, v32 offset:7280
	s_waitcnt vmcnt(7)
	ds_write_b32 v1, v22 offset:8320
	s_waitcnt vmcnt(6)
	ds_write_b32 v1, v23 offset:9360
	s_waitcnt vmcnt(5)
	ds_write_b32 v1, v24 offset:10400
	s_waitcnt vmcnt(4)
	ds_write_b32 v1, v33 offset:11440
	s_waitcnt vmcnt(3)
	ds_write_b32 v1, v34 offset:12480
	s_waitcnt vmcnt(2)
	ds_write_b32 v1, v35 offset:13520
	s_waitcnt vmcnt(1)
	ds_write_b32 v1, v36 offset:14560
	s_waitcnt vmcnt(0)
	ds_write_b32 v1, v37 offset:15600
	v_lshrrev_b32_e32 v28, 3, v0
	v_lshlrev_b32_e32 v6, 1, v8
	v_mul_u32_u24_e32 v8, 0x104, v8
	v_lshl_add_u32 v8, v28, 2, v8
	v_add_u32_e32 v9, 0x400, v8
	s_waitcnt lgkmcnt(0)
	s_barrier
	ds_read2_b32 v[10:11], v8 offset1:32
	ds_read2_b32 v[12:13], v8 offset0:130 offset1:162
	ds_read2_b32 v[14:15], v9 offset0:4 offset1:36
	ds_read2_b32 v[16:17], v9 offset0:134 offset1:166
	ds_read2_b32 v[18:19], v9 offset0:199 offset1:231
	ds_read2_b32 v[20:21], v9 offset0:69 offset1:101
	ds_read2_b32 v[22:23], v8 offset0:195 offset1:227
	ds_read2_b32 v[24:25], v8 offset0:65 offset1:97
	s_lshl_b32 s1, s1, 7
	s_add_u32 s4, s10, s1
	s_addc_u32 s5, s11, 0
	v_mov_b32_e32 v7, v3
	v_lshl_add_u64 v[6:7], s[4:5], 0, v[6:7]
	s_mov_b64 s[4:5], 0x600000
	v_lshl_add_u64 v[26:27], v[6:7], 0, s[4:5]
	s_waitcnt lgkmcnt(0)
	v_cvt_pk_f16_f32 v6, v10, v24
	v_or_b32_e32 v10, s0, v28
	v_lshlrev_b32_e32 v28, 11, v10
	v_mov_b32_e32 v29, v3
	v_cvt_pk_f16_f32 v9, v16, v18
	v_cvt_pk_f16_f32 v8, v14, v20
	v_cvt_pk_f16_f32 v7, v12, v22
	v_lshl_add_u64 v[30:31], v[26:27], 0, v[28:29]
	global_store_dwordx4 v[30:31], v[6:9], off
	v_or_b32_e32 v10, 0x10000, v28
	s_mov_b64 s[0:1], 0
	v_cvt_pk_f16_f32 v6, v11, v25
	v_mov_b32_e32 v11, v3
	v_cvt_pk_f16_f32 v9, v17, v19
	v_cvt_pk_f16_f32 v8, v15, v21
	v_cvt_pk_f16_f32 v7, v13, v23
	v_lshl_add_u64 v[10:11], v[26:27], 0, v[10:11]
	global_store_dwordx4 v[10:11], v[6:9], off
.LBB0_11:
	s_andn2_b64 vcc, exec, s[0:1]
	s_cbranch_vccnz .LBB0_13
	s_add_i32 s0, s2, 0xfa78
	s_and_b32 s1, s0, 0xffff
	s_mul_i32 s1, s1, 0xaaab
	s_lshr_b32 s1, s1, 20
	s_mul_i32 s3, s1, 24
	s_sub_i32 s0, s0, s3
	s_lshl_b32 s0, s0, 6
	s_and_b32 s0, s0, 0xffc0
	s_lshl_b32 s3, s1, 6
	s_waitcnt lgkmcnt(0)
	s_lshl_b32 s4, s0, 2
	s_add_u32 s4, s18, s4
	s_addc_u32 s5, s19, 0
	v_mov_b32_e32 v3, 0
	v_or_b32_e32 v22, s3, v5
	v_lshl_add_u64 v[6:7], s[4:5], 0, v[2:3]
	v_mul_u32_u24_e32 v2, 0x600, v22
	v_lshlrev_b32_e32 v2, 2, v2
	v_lshl_add_u64 v[8:9], v[6:7], 0, v[2:3]
	v_or_b32_e32 v2, s3, v4
	v_mul_u32_u24_e32 v2, 0x600, v2
	v_lshlrev_b32_e32 v2, 2, v2
	v_lshl_add_u64 v[4:5], v[6:7], 0, v[2:3]
	v_or_b32_e32 v2, 8, v22
	v_mul_u32_u24_e32 v2, 0x600, v2
	v_lshlrev_b32_e32 v2, 2, v2
	v_lshl_add_u64 v[10:11], v[6:7], 0, v[2:3]
	v_or_b32_e32 v2, 12, v22
	v_mul_u32_u24_e32 v2, 0x600, v2
	v_lshlrev_b32_e32 v2, 2, v2
	v_lshl_add_u64 v[12:13], v[6:7], 0, v[2:3]
	v_or_b32_e32 v2, 16, v22
	v_mul_u32_u24_e32 v2, 0x600, v2
	v_lshlrev_b32_e32 v2, 2, v2
	v_lshl_add_u64 v[14:15], v[6:7], 0, v[2:3]
	v_or_b32_e32 v2, 20, v22
	v_mul_u32_u24_e32 v2, 0x600, v2
	v_lshlrev_b32_e32 v2, 2, v2
	v_lshl_add_u64 v[16:17], v[6:7], 0, v[2:3]
	v_or_b32_e32 v2, 24, v22
	v_mul_u32_u24_e32 v2, 0x600, v2
	v_lshlrev_b32_e32 v2, 2, v2
	v_lshl_add_u64 v[18:19], v[6:7], 0, v[2:3]
	v_or_b32_e32 v2, 28, v22
	v_mul_u32_u24_e32 v2, 0x600, v2
	v_lshlrev_b32_e32 v2, 2, v2
	v_lshl_add_u64 v[20:21], v[6:7], 0, v[2:3]
	v_or_b32_e32 v2, 32, v22
	v_mul_u32_u24_e32 v2, 0x600, v2
	v_lshlrev_b32_e32 v2, 2, v2
	global_load_dword v23, v[8:9], off nt
	global_load_dword v24, v[4:5], off nt
	global_load_dword v25, v[10:11], off nt
	global_load_dword v26, v[12:13], off nt
	global_load_dword v27, v[14:15], off nt
	global_load_dword v28, v[16:17], off nt
	global_load_dword v29, v[18:19], off nt
	global_load_dword v30, v[20:21], off nt
	v_lshl_add_u64 v[4:5], v[6:7], 0, v[2:3]
	v_or_b32_e32 v2, 36, v22
	v_mul_u32_u24_e32 v2, 0x600, v2
	v_lshlrev_b32_e32 v2, 2, v2
	v_lshl_add_u64 v[8:9], v[6:7], 0, v[2:3]
	v_or_b32_e32 v2, 40, v22
	v_mul_u32_u24_e32 v2, 0x600, v2
	v_lshlrev_b32_e32 v2, 2, v2
	v_lshl_add_u64 v[10:11], v[6:7], 0, v[2:3]
	v_or_b32_e32 v2, 44, v22
	v_mul_u32_u24_e32 v2, 0x600, v2
	v_lshlrev_b32_e32 v2, 2, v2
	v_lshl_add_u64 v[12:13], v[6:7], 0, v[2:3]
	v_or_b32_e32 v2, 48, v22
	v_mul_u32_u24_e32 v2, 0x600, v2
	v_lshlrev_b32_e32 v2, 2, v2
	v_lshl_add_u64 v[14:15], v[6:7], 0, v[2:3]
	v_or_b32_e32 v2, 52, v22
	v_mul_u32_u24_e32 v2, 0x600, v2
	v_lshlrev_b32_e32 v2, 2, v2
	v_lshl_add_u64 v[16:17], v[6:7], 0, v[2:3]
	v_or_b32_e32 v2, 56, v22
	v_mul_u32_u24_e32 v2, 0x600, v2
	v_lshlrev_b32_e32 v2, 2, v2
	v_lshl_add_u64 v[18:19], v[6:7], 0, v[2:3]
	v_or_b32_e32 v2, 60, v22
	v_mul_u32_u24_e32 v2, 0x600, v2
	v_lshlrev_b32_e32 v2, 2, v2
	v_lshl_add_u64 v[6:7], v[6:7], 0, v[2:3]
	global_load_dword v2, v[4:5], off nt
	global_load_dword v20, v[8:9], off nt
	global_load_dword v21, v[10:11], off nt
	global_load_dword v22, v[12:13], off nt
	global_load_dword v31, v[14:15], off nt
	global_load_dword v32, v[16:17], off nt
	global_load_dword v33, v[18:19], off nt
	global_load_dword v34, v[6:7], off nt
	s_lshl_b32 s1, s1, 7
	s_add_u32 s4, s10, s1
	s_addc_u32 s5, s11, 0
	s_waitcnt vmcnt(15)
	ds_write_b32 v1, v23
	s_waitcnt vmcnt(14)
	ds_write_b32 v1, v24 offset:1040
	s_waitcnt vmcnt(13)
	ds_write_b32 v1, v25 offset:2080
	s_waitcnt vmcnt(12)
	ds_write_b32 v1, v26 offset:3120
	s_waitcnt vmcnt(11)
	ds_write_b32 v1, v27 offset:4160
	s_waitcnt vmcnt(10)
	ds_write_b32 v1, v28 offset:5200
	s_waitcnt vmcnt(9)
	ds_write_b32 v1, v29 offset:6240
	s_waitcnt vmcnt(8)
	ds_write_b32 v1, v30 offset:7280
	s_waitcnt vmcnt(7)
	ds_write_b32 v1, v2 offset:8320
	s_waitcnt vmcnt(6)
	ds_write_b32 v1, v20 offset:9360
	s_waitcnt vmcnt(5)
	ds_write_b32 v1, v21 offset:10400
	s_waitcnt vmcnt(4)
	ds_write_b32 v1, v22 offset:11440
	s_waitcnt vmcnt(3)
	ds_write_b32 v1, v31 offset:12480
	s_waitcnt vmcnt(2)
	ds_write_b32 v1, v32 offset:13520
	s_waitcnt vmcnt(1)
	ds_write_b32 v1, v33 offset:14560
	s_waitcnt vmcnt(0)
	ds_write_b32 v1, v34 offset:15600
	v_lshlrev_b32_e32 v2, 3, v0
	v_and_b32_e32 v6, 56, v2
	v_lshlrev_b32_e32 v2, 1, v6
	v_lshrrev_b32_e32 v1, 3, v0
	v_lshl_add_u64 v[4:5], s[4:5], 0, v[2:3]
	v_mul_u32_u24_e32 v2, 0x104, v6
	v_lshl_add_u32 v2, v1, 2, v2
	v_add_u32_e32 v6, 0x400, v2
	s_waitcnt lgkmcnt(0)
	s_barrier
	ds_read2_b32 v[8:9], v2 offset1:32
	ds_read2_b32 v[10:11], v2 offset0:130 offset1:162
	ds_read2_b32 v[12:13], v6 offset0:4 offset1:36
	ds_read2_b32 v[14:15], v6 offset0:134 offset1:166
	ds_read2_b32 v[16:17], v6 offset0:199 offset1:231
	ds_read2_b32 v[18:19], v6 offset0:69 offset1:101
	ds_read2_b32 v[20:21], v2 offset0:195 offset1:227
	ds_read2_b32 v[22:23], v2 offset0:65 offset1:97
	s_mov_b64 s[4:5], 0x300000
	v_or_b32_e32 v1, s0, v1
	v_lshl_add_u64 v[24:25], v[4:5], 0, s[4:5]
	v_lshlrev_b32_e32 v2, 11, v1
	s_waitcnt lgkmcnt(3)
	v_cvt_pk_f16_f32 v7, v14, v16
	s_waitcnt lgkmcnt(2)
	v_cvt_pk_f16_f32 v6, v12, v18
	s_waitcnt lgkmcnt(1)
	v_cvt_pk_f16_f32 v5, v10, v20
	s_waitcnt lgkmcnt(0)
	v_cvt_pk_f16_f32 v4, v8, v22
	v_lshl_add_u64 v[26:27], v[24:25], 0, v[2:3]
	v_or_b32_e32 v2, 0x10000, v2
	global_store_dwordx4 v[26:27], v[4:7], off
	v_lshl_add_u64 v[2:3], v[24:25], 0, v[2:3]
	s_nop 0
	v_cvt_pk_f16_f32 v7, v15, v17
	v_cvt_pk_f16_f32 v6, v13, v19
	v_cvt_pk_f16_f32 v5, v11, v21
	v_cvt_pk_f16_f32 v4, v9, v23
	global_store_dwordx4 v[2:3], v[4:7], off

.LBB0_14:
	s_andn2_b64 vcc, exec, s[0:1]
	s_cbranch_vccnz .LBB0_16
	s_add_i32 s0, s2, 56
	s_and_b32 s1, s0, 0xff
	s_mulk_i32 s1, 0xab
	s_bfe_u32 s1, s1, 0x5000b
	s_mul_i32 s3, s1, 12
	s_sub_i32 s0, s0, s3
	s_and_b32 s0, s0, 0xff
	s_lshl_b32 s3, s0, 8
	v_and_b32_e32 v1, 63, v0
	v_lshrrev_b32_e32 v8, 6, v0
	s_waitcnt lgkmcnt(0)
	s_add_u32 s4, s16, s3
	s_addc_u32 s5, s17, 0
	v_lshlrev_b32_e32 v6, 2, v1
	v_mov_b32_e32 v7, 0
	v_lshl_or_b32 v1, s1, 6, v8
	s_movk_i32 s3, 0x104
	v_lshl_add_u64 v[2:3], s[4:5], 0, v[6:7]
	v_mad_u32_u24 v22, v8, s3, v6
	v_or_b32_e32 v6, 4, v1
	v_mul_u32_u24_e32 v6, 0x300, v6
	v_lshlrev_b32_e32 v6, 2, v6
	v_lshl_add_u64 v[8:9], v[2:3], 0, v[6:7]
	v_or_b32_e32 v6, 8, v1
	v_mul_u32_u24_e32 v6, 0x300, v6
	v_lshlrev_b32_e32 v6, 2, v6
	v_lshl_add_u64 v[10:11], v[2:3], 0, v[6:7]
	v_or_b32_e32 v6, 12, v1
	v_mul_u32_u24_e32 v6, 0x300, v6
	v_lshlrev_b32_e32 v6, 2, v6
	v_lshl_add_u64 v[12:13], v[2:3], 0, v[6:7]
	v_or_b32_e32 v6, 16, v1
	v_mul_u32_u24_e32 v6, 0x300, v6
	v_lshlrev_b32_e32 v6, 2, v6
	v_lshl_add_u64 v[14:15], v[2:3], 0, v[6:7]
	v_or_b32_e32 v6, 20, v1
	v_mul_u32_u24_e32 v6, 0x300, v6
	v_lshlrev_b32_e32 v6, 2, v6
	v_lshl_add_u64 v[16:17], v[2:3], 0, v[6:7]
	v_or_b32_e32 v6, 24, v1
	v_mul_u32_u24_e32 v6, 0x300, v6
	v_lshlrev_b32_e32 v6, 2, v6
	v_mul_u32_u24_e32 v4, 0x300, v1
	v_lshl_add_u64 v[18:19], v[2:3], 0, v[6:7]
	v_or_b32_e32 v6, 28, v1
	v_lshlrev_b32_e32 v4, 2, v4
	v_mov_b32_e32 v5, v7
	v_mul_u32_u24_e32 v6, 0x300, v6
	v_lshl_add_u64 v[4:5], v[2:3], 0, v[4:5]
	v_lshlrev_b32_e32 v6, 2, v6
	v_lshl_add_u64 v[20:21], v[2:3], 0, v[6:7]
	global_load_dword v23, v[4:5], off nt
	global_load_dword v24, v[8:9], off nt
	global_load_dword v25, v[10:11], off nt
	global_load_dword v26, v[12:13], off nt
	global_load_dword v27, v[14:15], off nt
	global_load_dword v28, v[16:17], off nt
	global_load_dword v29, v[18:19], off nt
	global_load_dword v30, v[20:21], off nt
	v_or_b32_e32 v4, 32, v1
	v_mul_u32_u24_e32 v4, 0x300, v4
	v_lshlrev_b32_e32 v6, 2, v4
	v_lshl_add_u64 v[4:5], v[2:3], 0, v[6:7]
	v_or_b32_e32 v6, 36, v1
	v_mul_u32_u24_e32 v6, 0x300, v6
	v_lshlrev_b32_e32 v6, 2, v6
	v_lshl_add_u64 v[8:9], v[2:3], 0, v[6:7]
	v_or_b32_e32 v6, 40, v1
	v_mul_u32_u24_e32 v6, 0x300, v6
	v_lshlrev_b32_e32 v6, 2, v6
	v_lshl_add_u64 v[10:11], v[2:3], 0, v[6:7]
	v_or_b32_e32 v6, 44, v1
	v_mul_u32_u24_e32 v6, 0x300, v6
	v_lshlrev_b32_e32 v6, 2, v6
	v_lshl_add_u64 v[12:13], v[2:3], 0, v[6:7]
	v_or_b32_e32 v6, 48, v1
	v_mul_u32_u24_e32 v6, 0x300, v6
	v_lshlrev_b32_e32 v6, 2, v6
	v_lshl_add_u64 v[14:15], v[2:3], 0, v[6:7]
	v_or_b32_e32 v6, 52, v1
	v_mul_u32_u24_e32 v6, 0x300, v6
	v_lshlrev_b32_e32 v6, 2, v6
	v_lshl_add_u64 v[16:17], v[2:3], 0, v[6:7]
	v_or_b32_e32 v6, 56, v1
	v_mul_u32_u24_e32 v6, 0x300, v6
	v_or_b32_e32 v1, 60, v1
	v_lshlrev_b32_e32 v6, 2, v6
	v_mul_u32_u24_e32 v1, 0x300, v1
	v_lshl_add_u64 v[18:19], v[2:3], 0, v[6:7]
	v_lshlrev_b32_e32 v6, 2, v1
	v_lshl_add_u64 v[2:3], v[2:3], 0, v[6:7]
	global_load_dword v1, v[4:5], off nt
	global_load_dword v6, v[8:9], off nt
	global_load_dword v20, v[10:11], off nt
	global_load_dword v21, v[12:13], off nt
	global_load_dword v31, v[14:15], off nt
	global_load_dword v32, v[16:17], off nt
	global_load_dword v33, v[18:19], off nt
	global_load_dword v34, v[2:3], off nt
	v_lshlrev_b32_e32 v2, 3, v0
	v_and_b32_e32 v4, 56, v2
	s_lshl_b32 s1, s1, 7
	s_add_u32 s4, s10, s1
	s_addc_u32 s5, s11, 0
	s_waitcnt vmcnt(15)
	ds_write_b32 v22, v23
	s_waitcnt vmcnt(14)
	ds_write_b32 v22, v24 offset:1040
	s_waitcnt vmcnt(13)
	ds_write_b32 v22, v25 offset:2080
	s_waitcnt vmcnt(12)
	ds_write_b32 v22, v26 offset:3120
	s_waitcnt vmcnt(11)
	ds_write_b32 v22, v27 offset:4160
	s_waitcnt vmcnt(10)
	ds_write_b32 v22, v28 offset:5200
	s_waitcnt vmcnt(9)
	ds_write_b32 v22, v29 offset:6240
	s_waitcnt vmcnt(8)
	ds_write_b32 v22, v30 offset:7280
	s_waitcnt vmcnt(7)
	ds_write_b32 v22, v1 offset:8320
	s_waitcnt vmcnt(6)
	ds_write_b32 v22, v6 offset:9360
	s_waitcnt vmcnt(5)
	ds_write_b32 v22, v20 offset:10400
	s_waitcnt vmcnt(4)
	ds_write_b32 v22, v21 offset:11440
	s_waitcnt vmcnt(3)
	ds_write_b32 v22, v31 offset:12480
	s_waitcnt vmcnt(2)
	ds_write_b32 v22, v32 offset:13520
	s_waitcnt vmcnt(1)
	ds_write_b32 v22, v33 offset:14560
	s_waitcnt vmcnt(0)
	ds_write_b32 v22, v34 offset:15600
	v_lshrrev_b32_e32 v1, 3, v0
	v_lshlrev_b32_e32 v6, 1, v4
	v_mul_u32_u24_e32 v4, 0x104, v4
	v_lshl_add_u32 v4, v1, 2, v4
	v_add_u32_e32 v5, 0x400, v4
	s_waitcnt lgkmcnt(0)
	s_barrier
	ds_read2_b32 v[8:9], v4 offset1:32
	ds_read2_b32 v[10:11], v4 offset0:130 offset1:162
	ds_read2_b32 v[12:13], v5 offset0:4 offset1:36
	ds_read2_b32 v[14:15], v5 offset0:134 offset1:166
	ds_read2_b32 v[16:17], v5 offset0:199 offset1:231
	ds_read2_b32 v[18:19], v5 offset0:69 offset1:101
	ds_read2_b32 v[20:21], v4 offset0:195 offset1:227
	ds_read2_b32 v[22:23], v4 offset0:65 offset1:97
	v_lshl_add_u64 v[2:3], s[4:5], 0, v[6:7]
	s_mov_b64 s[4:5], 0x180000
	v_lshlrev_b32_e32 v1, 11, v1
	v_lshl_add_u64 v[24:25], v[2:3], 0, s[4:5]
	v_lshl_or_b32 v6, s0, 17, v1
	s_waitcnt lgkmcnt(3)
	v_cvt_pk_f16_f32 v5, v14, v16
	s_waitcnt lgkmcnt(2)
	v_cvt_pk_f16_f32 v4, v12, v18
	s_waitcnt lgkmcnt(1)
	v_cvt_pk_f16_f32 v3, v10, v20
	s_waitcnt lgkmcnt(0)
	v_cvt_pk_f16_f32 v2, v8, v22
	v_lshl_add_u64 v[26:27], v[24:25], 0, v[6:7]
	v_or_b32_e32 v6, 0x10000, v6
	global_store_dwordx4 v[26:27], v[2:5], off
	v_lshl_add_u64 v[6:7], v[24:25], 0, v[6:7]
	s_nop 0
	v_cvt_pk_f16_f32 v5, v15, v17
	v_cvt_pk_f16_f32 v4, v13, v19
	v_cvt_pk_f16_f32 v3, v11, v21
	v_cvt_pk_f16_f32 v2, v9, v23
	global_store_dwordx4 v[6:7], v[2:5], off

.LBB0_17:
	s_andn2_b64 vcc, exec, s[0:1]
	s_cbranch_vccnz .LBB0_19
	s_add_i32 s0, s2, 0xfff8
	s_and_b32 s1, s0, 0xff
	s_mulk_i32 s1, 0xab
	s_bfe_u32 s1, s1, 0x5000b
	s_mul_i32 s3, s1, 12
	s_sub_i32 s0, s0, s3
	s_and_b32 s0, s0, 0xff
	s_lshl_b32 s3, s0, 8
	v_and_b32_e32 v1, 63, v0
	v_lshrrev_b32_e32 v8, 6, v0
	s_waitcnt lgkmcnt(0)
	s_add_u32 s4, s14, s3
	s_addc_u32 s5, s15, 0
	v_lshlrev_b32_e32 v6, 2, v1
	v_mov_b32_e32 v7, 0
	v_lshl_or_b32 v1, s1, 6, v8
	s_movk_i32 s3, 0x104
	v_lshl_add_u64 v[2:3], s[4:5], 0, v[6:7]
	v_mad_u32_u24 v22, v8, s3, v6
	v_or_b32_e32 v6, 4, v1
	v_mul_u32_u24_e32 v6, 0x300, v6
	v_lshlrev_b32_e32 v6, 2, v6
	v_lshl_add_u64 v[8:9], v[2:3], 0, v[6:7]
	v_or_b32_e32 v6, 8, v1
	v_mul_u32_u24_e32 v6, 0x300, v6
	v_lshlrev_b32_e32 v6, 2, v6
	v_lshl_add_u64 v[10:11], v[2:3], 0, v[6:7]
	v_or_b32_e32 v6, 12, v1
	v_mul_u32_u24_e32 v6, 0x300, v6
	v_lshlrev_b32_e32 v6, 2, v6
	v_lshl_add_u64 v[12:13], v[2:3], 0, v[6:7]
	v_or_b32_e32 v6, 16, v1
	v_mul_u32_u24_e32 v6, 0x300, v6
	v_lshlrev_b32_e32 v6, 2, v6
	v_lshl_add_u64 v[14:15], v[2:3], 0, v[6:7]
	v_or_b32_e32 v6, 20, v1
	v_mul_u32_u24_e32 v6, 0x300, v6
	v_lshlrev_b32_e32 v6, 2, v6
	v_lshl_add_u64 v[16:17], v[2:3], 0, v[6:7]
	v_or_b32_e32 v6, 24, v1
	v_mul_u32_u24_e32 v6, 0x300, v6
	v_lshlrev_b32_e32 v6, 2, v6
	v_mul_u32_u24_e32 v4, 0x300, v1
	v_lshl_add_u64 v[18:19], v[2:3], 0, v[6:7]
	v_or_b32_e32 v6, 28, v1
	v_lshlrev_b32_e32 v4, 2, v4
	v_mov_b32_e32 v5, v7
	v_mul_u32_u24_e32 v6, 0x300, v6
	v_lshl_add_u64 v[4:5], v[2:3], 0, v[4:5]
	v_lshlrev_b32_e32 v6, 2, v6
	v_lshl_add_u64 v[20:21], v[2:3], 0, v[6:7]
	global_load_dword v23, v[4:5], off nt
	global_load_dword v24, v[8:9], off nt
	global_load_dword v25, v[10:11], off nt
	global_load_dword v26, v[12:13], off nt
	global_load_dword v27, v[14:15], off nt
	global_load_dword v28, v[16:17], off nt
	global_load_dword v29, v[18:19], off nt
	global_load_dword v30, v[20:21], off nt
	v_or_b32_e32 v4, 32, v1
	v_mul_u32_u24_e32 v4, 0x300, v4
	v_lshlrev_b32_e32 v6, 2, v4
	v_lshl_add_u64 v[4:5], v[2:3], 0, v[6:7]
	v_or_b32_e32 v6, 36, v1
	v_mul_u32_u24_e32 v6, 0x300, v6
	v_lshlrev_b32_e32 v6, 2, v6
	v_lshl_add_u64 v[8:9], v[2:3], 0, v[6:7]
	v_or_b32_e32 v6, 40, v1
	v_mul_u32_u24_e32 v6, 0x300, v6
	v_lshlrev_b32_e32 v6, 2, v6
	v_lshl_add_u64 v[10:11], v[2:3], 0, v[6:7]
	v_or_b32_e32 v6, 44, v1
	v_mul_u32_u24_e32 v6, 0x300, v6
	v_lshlrev_b32_e32 v6, 2, v6
	v_lshl_add_u64 v[12:13], v[2:3], 0, v[6:7]
	v_or_b32_e32 v6, 48, v1
	v_mul_u32_u24_e32 v6, 0x300, v6
	v_lshlrev_b32_e32 v6, 2, v6
	v_lshl_add_u64 v[14:15], v[2:3], 0, v[6:7]
	v_or_b32_e32 v6, 52, v1
	v_mul_u32_u24_e32 v6, 0x300, v6
	v_lshlrev_b32_e32 v6, 2, v6
	v_lshl_add_u64 v[16:17], v[2:3], 0, v[6:7]
	v_or_b32_e32 v6, 56, v1
	v_mul_u32_u24_e32 v6, 0x300, v6
	v_or_b32_e32 v1, 60, v1
	v_lshlrev_b32_e32 v6, 2, v6
	v_mul_u32_u24_e32 v1, 0x300, v1
	v_lshl_add_u64 v[18:19], v[2:3], 0, v[6:7]
	v_lshlrev_b32_e32 v6, 2, v1
	v_lshl_add_u64 v[2:3], v[2:3], 0, v[6:7]
	global_load_dword v1, v[4:5], off nt
	global_load_dword v6, v[8:9], off nt
	global_load_dword v20, v[10:11], off nt
	global_load_dword v21, v[12:13], off nt
	global_load_dword v31, v[14:15], off nt
	global_load_dword v32, v[16:17], off nt
	global_load_dword v33, v[18:19], off nt
	global_load_dword v34, v[2:3], off nt
	v_lshlrev_b32_e32 v2, 3, v0
	v_and_b32_e32 v2, 56, v2
	s_lshl_b32 s1, s1, 7
	s_add_u32 s4, s10, s1
	s_addc_u32 s5, s11, 0
	s_waitcnt vmcnt(15)
	ds_write_b32 v22, v23
	s_waitcnt vmcnt(14)
	ds_write_b32 v22, v24 offset:1040
	s_waitcnt vmcnt(13)
	ds_write_b32 v22, v25 offset:2080
	s_waitcnt vmcnt(12)
	ds_write_b32 v22, v26 offset:3120
	s_waitcnt vmcnt(11)
	ds_write_b32 v22, v27 offset:4160
	s_waitcnt vmcnt(10)
	ds_write_b32 v22, v28 offset:5200
	s_waitcnt vmcnt(9)
	ds_write_b32 v22, v29 offset:6240
	s_waitcnt vmcnt(8)
	ds_write_b32 v22, v30 offset:7280
	s_waitcnt vmcnt(7)
	ds_write_b32 v22, v1 offset:8320
	s_waitcnt vmcnt(6)
	ds_write_b32 v22, v6 offset:9360
	s_waitcnt vmcnt(5)
	ds_write_b32 v22, v20 offset:10400
	s_waitcnt vmcnt(4)
	ds_write_b32 v22, v21 offset:11440
	s_waitcnt vmcnt(3)
	ds_write_b32 v22, v31 offset:12480
	s_waitcnt vmcnt(2)
	ds_write_b32 v22, v32 offset:13520
	s_waitcnt vmcnt(1)
	ds_write_b32 v22, v33 offset:14560
	s_waitcnt vmcnt(0)
	ds_write_b32 v22, v34 offset:15600
	v_lshrrev_b32_e32 v1, 3, v0
	v_lshlrev_b32_e32 v6, 1, v2
	v_mul_u32_u24_e32 v2, 0x104, v2
	v_lshl_add_u32 v2, v1, 2, v2
	v_add_u32_e32 v3, 0x400, v2
	s_waitcnt lgkmcnt(0)
	s_barrier
	ds_read2_b32 v[8:9], v2 offset1:32
	ds_read2_b32 v[10:11], v2 offset0:130 offset1:162
	ds_read2_b32 v[12:13], v3 offset0:4 offset1:36
	ds_read2_b32 v[14:15], v3 offset0:134 offset1:166
	ds_read2_b32 v[16:17], v3 offset0:199 offset1:231
	ds_read2_b32 v[18:19], v3 offset0:69 offset1:101
	ds_read2_b32 v[20:21], v2 offset0:195 offset1:227
	ds_read2_b32 v[22:23], v2 offset0:65 offset1:97
	v_lshlrev_b32_e32 v1, 11, v1
	v_lshl_add_u64 v[24:25], s[4:5], 0, v[6:7]
	v_lshl_or_b32 v6, s0, 17, v1
	s_waitcnt lgkmcnt(3)
	v_cvt_pk_f16_f32 v5, v14, v16
	s_waitcnt lgkmcnt(2)
	v_cvt_pk_f16_f32 v4, v12, v18
	s_waitcnt lgkmcnt(1)
	v_cvt_pk_f16_f32 v3, v10, v20
	s_waitcnt lgkmcnt(0)
	v_cvt_pk_f16_f32 v2, v8, v22
	v_lshl_add_u64 v[26:27], v[24:25], 0, v[6:7]
	v_or_b32_e32 v6, 0x10000, v6
	global_store_dwordx4 v[26:27], v[2:5], off
	v_lshl_add_u64 v[6:7], v[24:25], 0, v[6:7]
	s_nop 0
	v_cvt_pk_f16_f32 v5, v15, v17
	v_cvt_pk_f16_f32 v4, v13, v19
	v_cvt_pk_f16_f32 v3, v11, v21
	v_cvt_pk_f16_f32 v2, v9, v23
	global_store_dwordx4 v[6:7], v[2:5], off

.LBB0_20:
	s_andn2_b64 vcc, exec, s[0:1]
	s_cbranch_vccnz .LBB0_22
	v_lshl_or_b32 v1, s2, 8, v0
	v_add_u32_e32 v10, 0xfffff800, v1
	v_mov_b32_e32 v11, 0
	v_lshlrev_b64 v[2:3], 5, v[10:11]
	s_waitcnt lgkmcnt(0)
	v_lshl_add_u64 v[12:13], s[12:13], 0, v[2:3]
	global_load_dwordx4 v[2:5], v[12:13], off nt
	global_load_dwordx4 v[6:9], v[12:13], off offset:16 nt
	v_mov_b32_e32 v12, s8
	v_mov_b32_e32 v13, s9
	s_waitcnt vmcnt(1)
	v_cvt_f16_f32_e32 v1, v2
	v_cvt_pk_f16_f32 v2, v3, v4
	s_waitcnt vmcnt(0)
	v_cvt_pk_f16_f32 v4, v5, v6
	v_cvt_f16_f32_e32 v6, v9
	v_cvt_pk_f16_f32 v5, v7, v8
	v_alignbit_b32 v3, v4, v2, 16
	v_alignbit_b32 v4, v5, v4, 16
	v_pack_b32_f16 v2, v1, v2
	v_alignbit_b32 v5, v6, v5, 16
	v_lshl_add_u64 v[6:7], v[10:11], 4, v[12:13]
	global_store_dwordx4 v[6:7], v[2:5], off
